# grid barrier: waiters poll the top-level generation word directly (XCD relay hop and its leader-side wait removed), on top of split/p8conv/lean/ln1fill/ln1sc1/earlyinv
# speedup vs baseline: 1.0006x; 1.0006x over previous
.LBB0_80:
	s_or_b64 exec, exec, s[8:9]
	buffer_inv sc1
	v_cvt_f32_u32_e32 v6, v4
	s_waitcnt vmcnt(0)
	v_readfirstlane_b32 s0, v5
	v_sub_u32_e32 v5, 0, v4
	v_rcp_iflag_f32_e32 v6, v6
	v_add_u32_e32 v7, s0, v3
	v_mul_f32_e32 v6, 0x4f7ffffe, v6
	v_cvt_u32_f32_e32 v6, v6
	v_mul_lo_u32 v3, v5, v6
	v_mul_hi_u32 v3, v6, v3
	v_add_u32_e32 v3, v6, v3
	v_mul_hi_u32 v3, v7, v3
	v_mul_lo_u32 v5, v3, v4
	v_sub_u32_e32 v5, v7, v5
	v_add_u32_e32 v6, 1, v3
	v_sub_u32_e32 v8, v5, v4
	v_cmp_ge_u32_e32 vcc, v5, v4
	s_nop 1
	v_cndmask_b32_e32 v3, v3, v6, vcc
	v_cndmask_b32_e32 v5, v5, v8, vcc
	v_add_u32_e32 v6, 1, v3
	v_cmp_ge_u32_e32 vcc, v5, v4
	v_add_u32_e32 v5, 1, v7
	s_nop 0
	v_cndmask_b32_e32 v3, v3, v6, vcc
	v_mul_lo_u32 v6, v4, v3
	v_add_u32_e32 v4, v6, v4
	v_cmp_ne_u32_e32 vcc, v5, v4
	s_and_saveexec_b64 s[0:1], vcc
	s_xor_b64 s[0:1], exec, s[0:1]
	s_cbranch_execz .LBB0_94
	s_waitcnt lgkmcnt(0)
	s_add_u32 s10, s4, 0x3500
	s_addc_u32 s11, s5, 0
	global_load_dword v2, v69, s[10:11] sc1
	s_waitcnt vmcnt(0)
	v_cmp_eq_u32_e32 vcc, v2, v3
	s_and_saveexec_b64 s[8:9], vcc
	s_cbranch_execz .LBB0_93
	s_mov_b32 s22, 1
	s_mov_b64 s[12:13], 0
	s_branch .LBB0_84

.LBB0_111:
	s_or_b64 exec, exec, s[0:1]
	s_mov_b64 s[0:1], exec
	v_mbcnt_lo_u32_b32 v2, s0, 0
	v_mbcnt_hi_u32_b32 v2, s1, v2
	v_cmp_eq_u32_e32 vcc, 0, v2
	s_waitcnt vmcnt(0)
	s_and_saveexec_b64 s[4:5], vcc
	s_cbranch_execz .LBB0_113
	s_bcnt1_i32_b64 s0, s[0:1]
	v_mov_b32_e32 v2, s0
.LBB0_113:
	s_or_b64 exec, exec, s[4:5]
	s_waitcnt vmcnt(0)

.LBB0_170:
	s_or_b64 exec, exec, s[0:1]
	s_mov_b64 s[0:1], exec
	v_mbcnt_lo_u32_b32 v2, s0, 0
	v_mbcnt_hi_u32_b32 v2, s1, v2
	v_cmp_eq_u32_e32 vcc, 0, v2
	s_waitcnt vmcnt(0)
	s_and_saveexec_b64 s[4:5], vcc
	s_cbranch_execz .LBB0_172
	s_bcnt1_i32_b64 s0, s[0:1]
	v_mov_b32_e32 v2, s0
.LBB0_172:
	s_or_b64 exec, exec, s[4:5]
	s_waitcnt vmcnt(0)

.LBB0_449:
	s_or_b64 exec, exec, s[8:9]
	buffer_inv sc1
	v_cvt_f32_u32_e32 v6, v4
	s_waitcnt vmcnt(0)
	v_readfirstlane_b32 s0, v5
	v_sub_u32_e32 v5, 0, v4
	v_rcp_iflag_f32_e32 v6, v6
	v_add_u32_e32 v7, s0, v3
	v_mul_f32_e32 v6, 0x4f7ffffe, v6
	v_cvt_u32_f32_e32 v6, v6
	v_mul_lo_u32 v3, v5, v6
	v_mul_hi_u32 v3, v6, v3
	v_add_u32_e32 v3, v6, v3
	v_mul_hi_u32 v3, v7, v3
	v_mul_lo_u32 v5, v3, v4
	v_sub_u32_e32 v5, v7, v5
	v_add_u32_e32 v6, 1, v3
	v_cmp_ge_u32_e32 vcc, v5, v4
	s_nop 1
	v_cndmask_b32_e32 v3, v3, v6, vcc
	v_sub_u32_e32 v6, v5, v4
	v_cndmask_b32_e32 v5, v5, v6, vcc
	v_add_u32_e32 v6, 1, v3
	v_cmp_ge_u32_e32 vcc, v5, v4
	v_add_u32_e32 v5, 1, v7
	s_nop 0
	v_cndmask_b32_e32 v3, v3, v6, vcc
	v_mul_lo_u32 v6, v4, v3
	v_add_u32_e32 v4, v6, v4
	v_cmp_ne_u32_e32 vcc, v5, v4
	s_and_saveexec_b64 s[0:1], vcc
	s_xor_b64 s[0:1], exec, s[0:1]
	s_cbranch_execz .LBB0_463
	s_waitcnt lgkmcnt(0)
	s_add_u32 s10, s4, 0x3500
	s_addc_u32 s11, s5, 0
	global_load_dword v2, v69, s[10:11] sc1
	s_waitcnt vmcnt(0)
	v_cmp_eq_u32_e32 vcc, v2, v3
	s_and_saveexec_b64 s[8:9], vcc
	s_cbranch_execz .LBB0_462
	s_mov_b32 s22, 1
	s_mov_b64 s[12:13], 0
	s_branch .LBB0_453

.LBB0_480:
	s_or_b64 exec, exec, s[0:1]
	s_mov_b64 s[0:1], exec
	v_mbcnt_lo_u32_b32 v2, s0, 0
	v_mbcnt_hi_u32_b32 v2, s1, v2
	v_cmp_eq_u32_e32 vcc, 0, v2
	s_waitcnt vmcnt(0)
	s_and_saveexec_b64 s[4:5], vcc
	s_cbranch_execz .LBB0_482
	s_bcnt1_i32_b64 s0, s[0:1]
	v_mov_b32_e32 v2, s0
.LBB0_482:
	s_or_b64 exec, exec, s[4:5]
	s_waitcnt vmcnt(0)

.LBB0_583:
	s_or_b64 exec, exec, s[0:1]
	s_mov_b64 s[0:1], exec
	v_mbcnt_lo_u32_b32 v2, s0, 0
	v_mbcnt_hi_u32_b32 v2, s1, v2
	v_cmp_eq_u32_e32 vcc, 0, v2
	s_waitcnt vmcnt(0)
	s_and_saveexec_b64 s[4:5], vcc
	s_cbranch_execz .LBB0_585
	s_bcnt1_i32_b64 s0, s[0:1]
	v_mov_b32_e32 v2, s0
.LBB0_585:
	s_or_b64 exec, exec, s[4:5]
	s_waitcnt vmcnt(0)

.LBB0_640:
	s_or_b64 exec, exec, s[0:1]
	s_mov_b64 s[0:1], exec
	v_mbcnt_lo_u32_b32 v2, s0, 0
	v_mbcnt_hi_u32_b32 v2, s1, v2
	v_cmp_eq_u32_e32 vcc, 0, v2
	s_waitcnt vmcnt(0)
	s_and_saveexec_b64 s[4:5], vcc
	s_cbranch_execz .LBB0_642
	s_bcnt1_i32_b64 s0, s[0:1]
	v_mov_b32_e32 v2, s0
.LBB0_642:
	s_or_b64 exec, exec, s[4:5]
	s_waitcnt vmcnt(0)

.LBB0_758:
	s_or_b64 exec, exec, s[0:1]
	s_mov_b64 s[0:1], exec
	v_mbcnt_lo_u32_b32 v2, s0, 0
	v_mbcnt_hi_u32_b32 v2, s1, v2
	v_cmp_eq_u32_e32 vcc, 0, v2
	s_waitcnt vmcnt(0)
	s_and_saveexec_b64 s[4:5], vcc
	s_cbranch_execz .LBB0_760
	s_bcnt1_i32_b64 s0, s[0:1]
	v_mov_b32_e32 v2, s0
.LBB0_760:
	s_or_b64 exec, exec, s[4:5]
	s_waitcnt vmcnt(0)

.LBB0_871:
	s_or_b64 exec, exec, s[0:1]
	s_mov_b64 s[0:1], exec
	v_mbcnt_lo_u32_b32 v2, s0, 0
	v_mbcnt_hi_u32_b32 v2, s1, v2
	v_cmp_eq_u32_e32 vcc, 0, v2
	s_waitcnt vmcnt(0)
	s_and_saveexec_b64 s[4:5], vcc
	s_cbranch_execz .LBB0_873
	s_bcnt1_i32_b64 s0, s[0:1]
	v_mov_b32_e32 v2, s0
.LBB0_873:
	s_or_b64 exec, exec, s[4:5]
	s_waitcnt vmcnt(0)

.LBB0_942:
	s_or_b64 exec, exec, s[0:1]
	s_mov_b64 s[0:1], exec
	v_mbcnt_lo_u32_b32 v2, s0, 0
	v_mbcnt_hi_u32_b32 v2, s1, v2
	v_cmp_eq_u32_e32 vcc, 0, v2
	s_waitcnt vmcnt(0)
	s_and_saveexec_b64 s[4:5], vcc
	s_cbranch_execz .LBB0_944
	s_bcnt1_i32_b64 s0, s[0:1]
	v_mov_b32_e32 v2, s0
.LBB0_944:
	s_or_b64 exec, exec, s[4:5]
	s_waitcnt vmcnt(0)

.LBB0_1011:
	s_or_b64 exec, exec, s[0:1]
	s_mov_b64 s[0:1], exec
	v_mbcnt_lo_u32_b32 v2, s0, 0
	v_mbcnt_hi_u32_b32 v2, s1, v2
	v_cmp_eq_u32_e32 vcc, 0, v2
	s_waitcnt vmcnt(0)
	s_and_saveexec_b64 s[4:5], vcc
	s_cbranch_execz .LBB0_1013
	s_bcnt1_i32_b64 s0, s[0:1]
	v_mov_b32_e32 v2, s0
.LBB0_1013:
	s_or_b64 exec, exec, s[4:5]
	s_waitcnt vmcnt(0)

.LBB0_1157:
	s_or_b64 exec, exec, s[0:1]
	s_mov_b64 s[0:1], exec
	v_mbcnt_lo_u32_b32 v2, s0, 0
	v_mbcnt_hi_u32_b32 v2, s1, v2
	v_cmp_eq_u32_e32 vcc, 0, v2
	s_waitcnt vmcnt(0)
	s_and_saveexec_b64 s[4:5], vcc
	s_cbranch_execz .LBB0_1159
	s_bcnt1_i32_b64 s0, s[0:1]
	v_mov_b32_e32 v2, s0
.LBB0_1159:
	s_or_b64 exec, exec, s[4:5]
	s_waitcnt vmcnt(0)

.LBB0_1295:
	s_or_b64 exec, exec, s[0:1]
	s_mov_b64 s[0:1], exec
	v_mbcnt_lo_u32_b32 v2, s0, 0
	v_mbcnt_hi_u32_b32 v2, s1, v2
	v_cmp_eq_u32_e32 vcc, 0, v2
	s_waitcnt vmcnt(0)
	s_and_saveexec_b64 s[4:5], vcc
	s_cbranch_execz .LBB0_1297
	s_bcnt1_i32_b64 s0, s[0:1]
	v_mov_b32_e32 v2, s0
.LBB0_1297:
	s_or_b64 exec, exec, s[4:5]
	s_waitcnt vmcnt(0)

.LBB0_1483:
	s_or_b64 exec, exec, s[8:9]
	v_cvt_f32_u32_e32 v6, v4
	s_waitcnt vmcnt(0)
	v_readfirstlane_b32 s0, v5
	v_sub_u32_e32 v5, 0, v4
	v_rcp_iflag_f32_e32 v6, v6
	v_add_u32_e32 v7, s0, v3
	v_mul_f32_e32 v6, 0x4f7ffffe, v6
	v_cvt_u32_f32_e32 v6, v6
	v_mul_lo_u32 v3, v5, v6
	v_mul_hi_u32 v3, v6, v3
	v_add_u32_e32 v3, v6, v3
	v_mul_hi_u32 v3, v7, v3
	v_mul_lo_u32 v5, v3, v4
	v_sub_u32_e32 v5, v7, v5
	v_add_u32_e32 v6, 1, v3
	v_cmp_ge_u32_e32 vcc, v5, v4
	s_nop 1
	v_cndmask_b32_e32 v3, v3, v6, vcc
	v_sub_u32_e32 v6, v5, v4
	v_cndmask_b32_e32 v5, v5, v6, vcc
	v_add_u32_e32 v6, 1, v3
	v_cmp_ge_u32_e32 vcc, v5, v4
	v_add_u32_e32 v5, 1, v7
	s_nop 0
	v_cndmask_b32_e32 v3, v3, v6, vcc
	v_mul_lo_u32 v6, v4, v3
	v_add_u32_e32 v4, v6, v4
	v_cmp_ne_u32_e32 vcc, v5, v4
	s_and_saveexec_b64 s[0:1], vcc
	s_xor_b64 s[0:1], exec, s[0:1]
	s_cbranch_execz .LBB0_1497
	s_waitcnt lgkmcnt(0)
	s_add_u32 s10, s4, 0x3500
	s_addc_u32 s11, s5, 0
	global_load_dword v2, v69, s[10:11] sc1
	s_waitcnt vmcnt(0)
	v_cmp_eq_u32_e32 vcc, v2, v3
	s_and_saveexec_b64 s[8:9], vcc
	s_cbranch_execz .LBB0_1496
	s_mov_b32 s22, 1
	s_mov_b64 s[12:13], 0
	s_branch .LBB0_1487

.LBB0_1514:
	s_or_b64 exec, exec, s[0:1]
	s_mov_b64 s[0:1], exec
	v_mbcnt_lo_u32_b32 v2, s0, 0
	v_mbcnt_hi_u32_b32 v2, s1, v2
	v_cmp_eq_u32_e32 vcc, 0, v2
	s_waitcnt vmcnt(0)
	buffer_inv sc1
	s_and_saveexec_b64 s[4:5], vcc
	s_cbranch_execz .LBB0_1516
	s_bcnt1_i32_b64 s0, s[0:1]
	v_mov_b32_e32 v2, s0
.LBB0_1516:
	s_or_b64 exec, exec, s[4:5]
	s_waitcnt vmcnt(0)

.LBB0_1669:
	s_or_b64 exec, exec, s[0:1]
	s_mov_b64 s[0:1], exec
	v_mbcnt_lo_u32_b32 v2, s0, 0
	v_mbcnt_hi_u32_b32 v2, s1, v2
	v_cmp_eq_u32_e32 vcc, 0, v2
	s_waitcnt vmcnt(0)
	s_and_saveexec_b64 s[4:5], vcc
	s_cbranch_execz .LBB0_1671
	s_bcnt1_i32_b64 s0, s[0:1]
	v_mov_b32_e32 v2, s0
.LBB0_1671:
	s_or_b64 exec, exec, s[4:5]
	s_waitcnt vmcnt(0)
